# P4 queues: next-item atomic pull issued ahead of the current item's epilogue
# baseline (speedup 1.0000x reference)
; template <bool MLA>
; __device__ __forceinline__ void attn_unit(char* lds, int h, int qb, const bf16_t* Qp, int ldq, const bf16_t* Kp, int ldk, const bf16_t* KRp, const bf16_t* Vp, int ldv,
;                                           unsigned char* Op, int ldo, const float* KMp, const float* rel_bias) {
;     ...
;     const int tid = threadIdx.x, wid = __builtin_amdgcn_readfirstlane(tid >> 6), lane = tid & 63, r32 = lane & 31, hi = lane >> 5;
;     float* wsf = (float*)(lds + OFF_WS) + wid * 64; float* li_l = wsf; float* al_l = wsf + 32; const float* al_h = al_l + 4 * hi; const float* li_h = li_l + 4 * hi;
;     unsigned* sel_l = (unsigned*)(lds + OFF_SEL); float* bt_l = (float*)(lds + OFF_BT); float* km_l = (float*)(lds + OFF_KM);
;     const int q0 = qb * 256, qlo = q0 + wid * 32, qpos = qlo + r32, NT = (qb + 1) * 4;
;     unsigned offKn[2], offV[2], offKr;
; #pragma unroll
;     for (int i = 0; i < 2; ++i) { const int pc = wid * 2 + i;
;         { const int row = pc * 4 + (lane >> 4), colB = ((lane & 15) * 16) ^ ((row & 7) << 4); offKn[i] = (unsigned)(row * ldk + (colB >> 1)); }
;         { const int sub = pc * 2 + (lane >> 5), kk = (sub >> 2) * 8 + ((lane & 31) >> 2), c = (sub & 3) * 32 + (lane & 3) * 8; const int k = (kk & ~0xC) | ((kk & 4) << 1) | ((kk & 8) >> 1);
;           offV[i] = (unsigned)(k * ldv + c); } }
;     { const int row = wid * 8 + (lane >> 3), colB = ((lane & 7) * 16) ^ ((row & 7) << 4); offKr = (unsigned)(row * 64 + (colB >> 1)); }
; __global__ void __launch_bounds__(512, 2) mega_fwd(Args args) {
;     ...
;         for (;;) { if (tid == 0) MISC[12] = atomicAdd(ctl + CW_AQ1, 1u);
;             __syncthreads(); const int it = (int)MISC[12]; __syncthreads();
;             if (it >= 512) break;
;             const int qb = 15 - (it >> 5), bh = it & 31, b = bh >> 3, hh = bh & 7;
.LBB0_1373:
	s_add_u32 s70, s18, 0x4a000000
	s_addc_u32 s71, s19, 0
	s_cmp_lt_i32 s20, 5
	s_cselect_b64 s[4:5], -1, 0
	s_cmp_gt_i32 s21, 4
	s_cselect_b64 s[6:7], -1, 0
	s_and_b64 s[36:37], s[4:5], s[6:7]
	s_andn2_b64 vcc, exec, s[36:37]
	s_cbranch_vccnz .LBB0_1778
	v_lshrrev_b32_e32 v186, 4, v164
	s_waitcnt vmcnt(15)
	v_and_b32_e32 v2, 15, v0
	v_bitop3_b32 v2, v186, v2, 4 bitop3:0x36
	v_bitop3_b32 v4, v186, v0, 15 bitop3:0x78
	v_lshlrev_b32_e32 v193, 3, v2
	v_lshrrev_b32_e32 v2, 3, v164
	v_lshlrev_b32_e32 v191, 3, v4
	v_bitop3_b32 v4, v2, v0, 7 bitop3:0x78
	v_lshrrev_b32_e32 v3, 5, v164
	v_lshlrev_b32_e32 v4, 3, v4
	v_lshl_or_b32 v158, v2, 6, v4
	v_lshlrev_b32_e32 v4, 4, v3
	s_waitcnt lgkmcnt(0)
	v_lshlrev_b32_e32 v5, 4, v0
	s_movk_i32 s3, 0x70
	s_add_u32 s8, s18, 0xc300
	s_waitcnt vmcnt(14)
	v_and_b32_e32 v6, 0x70, v5
	v_bitop3_b32 v154, v4, v5, s3 bitop3:0x78
	s_movk_i32 s3, 0x60
	s_addc_u32 s9, s19, 0
	v_bitop3_b32 v155, v4, v6, 32 bitop3:0x36
	v_bitop3_b32 v156, v4, v6, 64 bitop3:0x36
	v_bitop3_b32 v157, v4, v6, s3 bitop3:0x36
	v_and_b32_e32 v4, 0xc0, v5
	v_lshlrev_b32_e32 v5, 1, v0
	v_and_b32_e32 v168, 31, v0
	v_lshlrev_b32_e32 v165, 2, v3
	v_lshlrev_b32_e32 v152, 3, v0
	v_and_b32_e32 v5, 32, v5
	s_movk_i32 s3, 0x118
	s_cmp_lg_u32 0, -1
	v_lshlrev_b32_e32 v2, 3, v3
	v_and_or_b32 v5, v152, s3, v5
	s_cselect_b32 s3, 0, 0
	v_lshlrev_b32_e32 v170, 13, v3
	v_sub_u32_e32 v3, v168, v165
	v_and_b32_e32 v150, 32, v0
	v_and_b32_e32 v151, 24, v152
	v_lshrrev_b32_e32 v189, 1, v0
	v_mov_b32_e32 v147, 0
	v_mov_b32_e32 v7, 0x10000
	v_add3_u32 v194, v4, s3, v5
	v_and_b32_e32 v4, 3, v0
	v_add_u32_e32 v160, 0xee5, v3
	s_add_i32 s3, 0, 0x25170
	v_mbcnt_lo_u32_b32 v3, -1, 0
	v_bfe_u32 v187, v0, 2, 3
	v_or_b32_e32 v188, v150, v151
	v_and_b32_e32 v190, 8, v189
	v_or_b32_e32 v192, 4, v186
	v_lshlrev_b32_e32 v153, 8, v168
	v_lshl_or_b32 v159, v168, 7, v7
	v_cmp_gt_u32_e64 s[4:5], 32, v164
	s_mov_b32 s11, 0
	v_cmp_eq_u32_e64 s[6:7], 0, v4
	v_mov_b32_e32 v169, v147
	v_mov_b32_e32 v171, v147
	v_mov_b32_e32 v161, s3
	s_movk_i32 s16, 0x1ff
	s_movk_i32 s17, 0xc00
	s_mov_b64 s[38:39], 0x100
	s_mov_b64 s[40:41], 0x180
	s_mov_b32 s26, 0x41000000
	v_mbcnt_hi_u32_b32 v195, -1, v3
	v_mov_b32_e32 v162, 0x1ffff3
	v_lshlrev_b32_e32 v172, 1, v2
	v_mov_b32_e32 v163, 0xff800000
	s_mov_b64 s[98:99], exec
	s_and_b64 exec, exec, s[14:15]
	v_mov_b32_e32 v254, 0
	v_mov_b32_e32 v253, 1
	s_nop 0
	global_atomic_add v253, v254, v253, s[8:9] sc0
	s_mov_b64 exec, s[98:99]
	s_branch .LBB0_1377

; __global__ void __launch_bounds__(512, 2) mega_fwd(Args args) {
;     ...
;         for (;;) { if (tid == 0) MISC[12] = atomicAdd(ctl + CW_AQ1, 1u);
;             __syncthreads(); const int it = (int)MISC[12]; __syncthreads();
.LBB0_1380:
	s_or_b64 exec, exec, s[44:45]
	s_waitcnt vmcnt(0)
	v_readfirstlane_b32 s10, v253
	v_mov_b32_e32 v3, s3
	s_nop 0
	v_add_u32_e32 v2, s10, v2
	ds_write_b32 v3, v2

; #define LDS_WAIT() asm volatile("s_waitcnt lgkmcnt(0)" ::: "memory")
; __device__ __forceinline__ unsigned cvt4_fp8(float a, float b, float c, float d) { int w = 0; w = __builtin_amdgcn_cvt_pk_fp8_f32(a, b, w, false); w = __builtin_amdgcn_cvt_pk_fp8_f32(c, d, w, true); return (unsigned)w; }
; template <bool MLA>
; __device__ __forceinline__ void attn_unit(char* lds, int h, int qb, const bf16_t* Qp, int ldq, const bf16_t* Kp, int ldk, const bf16_t* KRp, const bf16_t* Vp, int ldv,
;                                           unsigned char* Op, int ldo, const float* KMp, const float* rel_bias) {
;     ...
;     if (hi == 0) li_l[r32] = l_reg; LDS_WAIT();
;     unsigned char* Ow = Op + (size_t)qlo * ldo;
; #pragma unroll
;     for (int r = 0; r < 16; ++r) { const int orow = CROWC(r) + 4 * hi; const float rl = 16.0f * __builtin_amdgcn_rcpf(li_h[CROWC(r)]);
; #pragma unroll
;         for (int d0 = 0; d0 < 4; ++d0) { const float v = o[d0][r] * rl; const float v1 = __shfl_xor(v, 1), v2 = __shfl_xor(v, 2), v3 = __shfl_xor(v1, 2);
;             if ((r32 & 3) == 0) *(unsigned*)(Ow + (size_t)orow * ldo + d0 * 32 + r32) = cvt4_fp8(v, v1, v2, v3); } }
; __global__ void __launch_bounds__(512, 2) mega_fwd(Args args) {
;     ...
;         for (;;) { if (tid == 0) MISC[12] = atomicAdd(ctl + CW_AQ1, 1u);
.LBB0_1394:
	s_mov_b64 s[98:99], exec
	s_and_b64 exec, exec, s[14:15]
	v_mov_b32_e32 v254, 0
	v_mov_b32_e32 v253, 1
	s_nop 0
	global_atomic_add v253, v254, v253, s[8:9] sc0
	s_mov_b64 exec, s[98:99]
	s_and_saveexec_b64 s[44:45], s[4:5]
	ds_write_b32 v173, v178
	s_or_b64 exec, exec, s[44:45]
	s_waitcnt lgkmcnt(0)
	ds_read_b32 v66, v167
	v_and_b32_e32 v68, 64, v195
	v_xor_b32_e32 v67, 1, v195
	v_add_u32_e32 v72, 64, v68
	v_cmp_lt_i32_e32 vcc, v67, v72
	s_waitcnt lgkmcnt(0)
	v_rcp_f32_e32 v66, v66
	s_lshl_b32 s10, s27, 7
	v_cndmask_b32_e32 v67, v195, v67, vcc
	v_lshlrev_b32_e32 v68, 2, v67
	v_mul_f32_e32 v69, 0x41800000, v66
	v_mul_f32_e32 v70, v34, v69
	s_nop 1
	v_mov_b32_dpp v71, v70 quad_perm:[1,0,3,2] row_mask:0xf bank_mask:0xf
	v_xor_b32_e32 v67, 2, v195
	s_add_u32 s22, s70, s43
	v_cmp_lt_i32_e32 vcc, v67, v72
	s_addc_u32 s23, s71, 0
	s_add_u32 s10, s22, s10
	v_cndmask_b32_e32 v34, v195, v67, vcc
	s_mov_b32 s43, s11
	v_lshlrev_b32_e32 v34, 2, v34
	s_addc_u32 s22, s23, 0
	s_lshl_b64 s[42:43], s[42:43], 11
	s_nop 1
	v_mov_b32_dpp v72, v70 quad_perm:[2,3,0,1] row_mask:0xf bank_mask:0xf
	s_waitcnt lgkmcnt(0)
	s_nop 1
	v_mov_b32_dpp v73, v71 quad_perm:[2,3,0,1] row_mask:0xf bank_mask:0xf
	s_add_u32 s42, s10, s42
	s_addc_u32 s43, s22, s43
	v_lshl_add_u64 v[66:67], s[42:43], 0, v[168:169]
	v_lshl_add_u64 v[66:67], v[66:67], 0, v[170:171]
	s_and_saveexec_b64 s[42:43], s[6:7]
	s_cbranch_execz .LBB0_1398
	v_mov_b32_e32 v74, v147
	v_cvt_pk_fp8_f32 v74, v70, v71
	s_waitcnt lgkmcnt(0)
	v_cvt_pk_fp8_f32 v74, v72, v73 op_sel:[0,0,1]
	global_store_dword v[66:67], v74, off

; template <bool MLA>
; __device__ __forceinline__ void attn_unit(char* lds, int h, int qb, const bf16_t* Qp, int ldq, const bf16_t* Kp, int ldk, const bf16_t* KRp, const bf16_t* Vp, int ldv,
;                                           unsigned char* Op, int ldo, const float* KMp, const float* rel_bias) {
;     ...
;         if (tid <= 128) { const int n = tid; int bk; if (n < 16) bk = n; else { const float v = logf((float)n * (1.0f / 16.0f)) / logf(8.0f) * 16.0f; bk = 16 + (int)v; if (bk > 31) bk = 31; }
;             bt_l[tid] = rel_bias[bk * 8 + h] * (1.0f / SCALE); }
;         for (int i = tid; i < 16 * 128; i += 512) km_l[i] = KMp[i] + KMp[i + 65536];
; __global__ void __launch_bounds__(512, 2) mega_fwd(Args args) {
;     ...
;         for (;;) { if (tid == 0) MISC[12] = atomicAdd(ctl + CW_AQ2, 1u);
;             __syncthreads(); const int it = (int)MISC[12]; __syncthreads();
;             if (it >= 512) break;
;             const int qb = 15 - (it >> 5), bh = it & 31, b = bh >> 3, hh = bh & 7;
.LBB0_1524:
	v_cvt_f32_u32_e32 v2, v0
	s_mov_b32 s3, 0x800000
	s_mov_b32 s8, 0x7f800000
	s_load_dwordx2 s[40:41], s[0:1], 0x58
	v_mul_f32_e32 v2, 0x3d800000, v2
	v_cmp_gt_f32_e32 vcc, s3, v2
	s_mov_b32 s3, 0x3f317217
	s_mov_b64 s[12:13], 0x200000
	v_cndmask_b32_e64 v3, 0, 32, vcc
	v_ldexp_f32 v2, v2, v3
	v_log_f32_e32 v2, v2
	v_mov_b32_e32 v3, 0x41b17218
	v_cndmask_b32_e32 v3, 0, v3, vcc
	s_add_u32 s38, s18, 0xc400
	v_mul_f32_e32 v4, 0x3f317217, v2
	v_fma_f32 v4, v2, s3, -v4
	v_fmamk_f32 v4, v2, 0x3377d1cf, v4
	v_fmac_f32_e32 v4, 0x3f317217, v2
	v_cmp_lt_f32_e64 s[8:9], |v2|, s8
	s_mov_b32 s3, 0x40051592
	s_addc_u32 s39, s19, 0
	v_cndmask_b32_e64 v2, v2, v4, s[8:9]
	v_sub_f32_e32 v2, v2, v3
	v_div_scale_f32 v3, s[8:9], s3, s3, v2
	v_rcp_f32_e32 v4, v3
	s_add_i32 s16, 0, 0x14c00
	s_add_i32 s58, 0, 0x25170
	s_mov_b32 s43, 0
	v_fma_f32 v5, -v3, v4, 1.0
	v_fmac_f32_e32 v4, v5, v4
	v_div_scale_f32 v5, vcc, v2, s3, v2
	v_mul_f32_e32 v6, v5, v4
	v_fma_f32 v7, -v3, v6, v5
	v_fmac_f32_e32 v6, v7, v4
	v_fma_f32 v3, -v3, v6, v5
	v_div_fmas_f32 v3, v3, v4, v6
	v_div_fixup_f32 v2, v3, s3, v2
	v_mul_f32_e32 v2, 0x41800000, v2
	v_cvt_i32_f32_e32 v2, v2
	v_mov_b32_e32 v3, 0x80
	v_cmp_gt_u32_e32 vcc, 16, v0
	v_and_b32_e32 v6, 1, v0
	v_min_i32_e32 v2, 15, v2
	v_lshl_add_u32 v4, v2, 3, v3
	v_mov_b32_e32 v3, 0
	v_mov_b32_e32 v167, v3
	v_cndmask_b32_e32 v202, v4, v152, vcc
	v_lshl_add_u64 v[4:5], s[18:19], 0, v[166:167]
	v_lshl_add_u64 v[174:175], v[4:5], 0, s[12:13]
	v_lshl_add_u32 v4, v6, 8, 0
	s_movk_i32 s3, 0x81
	v_add_u32_e32 v167, 0x15000, v4
	v_mul_u32_u24_e32 v4, 0x2100, v186
	v_cmp_gt_u32_e64 s[8:9], s3, v0
	v_lshlrev_b32_e32 v2, 6, v6
	s_add_i32 s3, 0, 0x14800
	v_or_b32_e32 v210, v4, v191
	v_or_b32_e32 v4, v4, v193
	v_add_u32_e32 v196, s16, v166
	v_cmp_eq_u32_e64 s[10:11], 0, v6
	v_lshl_add_u32 v197, v189, 2, s3
	v_lshl_add_u32 v198, v168, 2, s3
	v_or_b32_e32 v199, 1, v165
	v_or_b32_e32 v200, 2, v165
	v_or_b32_e32 v201, 3, v165
	v_add_u32_e32 v203, v154, v153
	v_add_u32_e32 v204, v155, v153
	v_add_u32_e32 v205, v156, v153
	v_add_u32_e32 v206, v157, v153
	v_or_b32_e32 v207, 0xfffffe00, v0
	v_add_u32_e32 v1, 0x15000, v1
	v_sub_u32_e32 v208, v168, v165
	v_add_u32_e32 v209, v150, v151
	s_movk_i32 s17, 0x2100
	v_add_u32_e32 v211, 0x8400, v4
	v_mov_b32_e32 v212, s58
	s_movk_i32 s59, 0x1ff
	s_movk_i32 s60, 0x4200
	s_mov_b64 s[44:45], 0x800
	s_movk_i32 s61, 0x5ff
	v_lshlrev_b32_e32 v176, 1, v2
	s_mov_b64 s[46:47], 0x31109800
	s_mov_b64 s[48:49], 0x31109880
	s_add_i32 s62, 0, 0x14e00
	s_mov_b32 s63, 0x41000000
	s_mov_b64 s[50:51], 0x400
	v_mov_b32_e32 v213, 0x1ffffff3
	v_mov_b64_e32 v[178:179], 0x31109000
	v_mov_b32_e32 v214, 0xa0
	v_mov_b32_e32 v215, 0xff800000
	s_mov_b64 s[98:99], exec
	s_and_b64 exec, exec, s[14:15]
	v_mov_b32_e32 v254, 0
	v_mov_b32_e32 v253, 1
	s_nop 0
	global_atomic_add v253, v254, v253, s[38:39] sc0
	s_mov_b64 exec, s[98:99]
	s_branch .LBB0_1527

; __global__ void __launch_bounds__(512, 2) mega_fwd(Args args) {
;     ...
;         for (;;) { if (tid == 0) MISC[12] = atomicAdd(ctl + CW_AQ2, 1u);
;             __syncthreads(); const int it = (int)MISC[12]; __syncthreads();
.LBB0_1530:
	s_or_b64 exec, exec, s[52:53]
	s_waitcnt vmcnt(0)
	v_readfirstlane_b32 s3, v253
	v_mov_b32_e32 v4, s58
	s_nop 0
	v_add_u32_e32 v2, s3, v2
	ds_write_b32 v4, v2

; #define LDS_WAIT() asm volatile("s_waitcnt lgkmcnt(0)" ::: "memory")
; __device__ __forceinline__ unsigned cvt4_fp8(float a, float b, float c, float d) { int w = 0; w = __builtin_amdgcn_cvt_pk_fp8_f32(a, b, w, false); w = __builtin_amdgcn_cvt_pk_fp8_f32(c, d, w, true); return (unsigned)w; }
; template <bool MLA>
; __device__ __forceinline__ void attn_unit(char* lds, int h, int qb, const bf16_t* Qp, int ldq, const bf16_t* Kp, int ldk, const bf16_t* KRp, const bf16_t* Vp, int ldv,
;                                           unsigned char* Op, int ldo, const float* KMp, const float* rel_bias) {
;     ...
;     if (hi == 0) li_l[r32] = l_reg; LDS_WAIT();
;     unsigned char* Ow = Op + (size_t)qlo * ldo;
; #pragma unroll
;     for (int r = 0; r < 16; ++r) { const int orow = CROWC(r) + 4 * hi; const float rl = 16.0f * __builtin_amdgcn_rcpf(li_h[CROWC(r)]);
; #pragma unroll
;         for (int d0 = 0; d0 < 4; ++d0) { const float v = o[d0][r] * rl; const float v1 = __shfl_xor(v, 1), v2 = __shfl_xor(v, 2), v3 = __shfl_xor(v1, 2);
;             if ((r32 & 3) == 0) *(unsigned*)(Ow + (size_t)orow * ldo + d0 * 32 + r32) = cvt4_fp8(v, v1, v2, v3); } }
; __global__ void __launch_bounds__(512, 2) mega_fwd(Args args) {
;     ...
;         for (;;) { if (tid == 0) MISC[12] = atomicAdd(ctl + CW_AQ2, 1u);
.LBB0_1645:
	s_waitcnt vmcnt(0)
	s_barrier
	s_mov_b64 s[98:99], exec
	s_and_b64 exec, exec, s[14:15]
	v_mov_b32_e32 v254, 0
	v_mov_b32_e32 v253, 1
	s_nop 0
	global_atomic_add v253, v254, v253, s[38:39] sc0
	s_mov_b64 exec, s[98:99]
	s_and_saveexec_b64 s[12:13], s[4:5]
	ds_write_b32 v177, v216
	s_or_b64 exec, exec, s[12:13]
	s_waitcnt lgkmcnt(0)
	ds_read_b32 v2, v173
	v_and_b32_e32 v69, 64, v195
	v_xor_b32_e32 v68, 1, v195
	v_add_u32_e32 v69, 64, v69
	v_cmp_lt_i32_e32 vcc, v68, v69
	s_waitcnt lgkmcnt(0)
	v_rcp_f32_e32 v70, v2
	s_lshl_b32 s12, s64, 11
	v_cndmask_b32_e32 v2, v195, v68, vcc
	v_lshlrev_b32_e32 v2, 2, v2
	v_mul_f32_e32 v72, 0x41800000, v70
	v_mul_f32_e32 v73, v52, v72
	s_nop 1
	v_mov_b32_dpp v74, v73 quad_perm:[1,0,3,2] row_mask:0xf bank_mask:0xf
	s_add_u32 s12, s70, s12
	v_xor_b32_e32 v68, 2, v195
	s_addc_u32 s13, s71, 0
	v_cmp_lt_i32_e32 vcc, v68, v69
	s_add_u32 s3, s12, s3
	s_addc_u32 s22, s13, 0
	v_cndmask_b32_e32 v52, v195, v68, vcc
	s_lshl_b64 s[12:13], s[42:43], 11
	v_lshlrev_b32_e32 v52, 2, v52
	s_add_u32 s12, s3, s12
	s_nop 1
	v_mov_b32_dpp v75, v73 quad_perm:[2,3,0,1] row_mask:0xf bank_mask:0xf
	s_waitcnt lgkmcnt(0)
	s_nop 1
	v_mov_b32_dpp v76, v74 quad_perm:[2,3,0,1] row_mask:0xf bank_mask:0xf
	s_addc_u32 s13, s22, s13
	v_lshl_add_u64 v[68:69], s[12:13], 0, v[168:169]
	v_lshl_add_u64 v[70:71], v[68:69], 0, v[170:171]
	v_lshl_add_u64 v[68:69], v[70:71], 0, s[50:51]
	s_and_saveexec_b64 s[12:13], s[6:7]
	s_cbranch_execz .LBB0_1649
	v_mov_b32_e32 v77, v3
	v_cvt_pk_fp8_f32 v77, v73, v74
	s_waitcnt lgkmcnt(0)
	v_cvt_pk_fp8_f32 v77, v75, v76 op_sel:[0,0,1]
	global_store_dword v[68:69], v77, off
